# K1 scan with a dynamic chunk queue: 16 work counters in the zeroed stats2 area (agg block 0 re-zeroes them), 16KiB chunks requested two ahead; ring 16; pipelined f32 GEMM
# speedup vs baseline: 1.0675x; 1.0551x over previous
.Lk1_scan:
	s_load_dwordx2 s[4:5], s[0:1], 0x0
	s_load_dwordx4 s[8:11], s[0:1], 0x20
	s_load_dwordx2 s[12:13], s[0:1], 0x30
	v_and_b32_e32 v6, 63, v0
	v_readfirstlane_b32 s3, v0
	v_lshlrev_b32_e32 v1, 4, v6
	v_lshlrev_b32_e32 v2, 2, v6
	v_or_b32_e32 v3, 1, v2
	v_or_b32_e32 v4, 2, v2
	v_or_b32_e32 v5, 3, v2
	s_lshr_b32 s3, s3, 6
	s_sub_u32 s16, s2, 0x60
	s_lshl_b32 s16, s16, 2
	s_add_u32 s16, s16, s3
	s_mul_i32 s17, s16, 0x48000
	s_lshr_b32 s18, s17, 2
	s_lshl_b32 s24, s3, 13
	s_mov_b32 s25, s24
	s_mov_b32 s28, s24
	s_mov_b32 s36, 0
	v_mov_b32_e32 v21, 1
	s_mov_b32 s27, 0
	s_mov_b32 s29, 0x55555556
	s_mov_b32 s31, 0xc0000
	s_waitcnt lgkmcnt(0)
	s_and_b32 s50, s16, 15
	s_lshr_b32 s51, s16, 4
	s_mul_i32 s52, s50, 2304
	s_lshl_b32 s53, s50, 6
	s_add_u32 s53, s53, 0xe000
	s_add_u32 s54, s10, s53
	s_addc_u32 s55, s11, 0
	s_add_u32 s57, s52, s51
	s_mul_i32 s57, s57, 0x4000
	s_lshr_b32 s18, s57, 2
	s_add_u32 s6, s4, s57
	s_addc_u32 s7, s5, 0
	v_mov_b32_e32 v27, 0
	s_mov_b64 exec, 1
	global_atomic_add v26, v27, v21, s[54:55] sc0
	s_mov_b64 exec, -1
	global_load_dwordx4 v[28:31], v1, s[6:7] nt
	s_add_u32 s6, s6, 0x400
	s_addc_u32 s7, s7, 0
	global_load_dwordx4 v[32:35], v1, s[6:7] nt
	s_add_u32 s6, s6, 0x400
	s_addc_u32 s7, s7, 0
	global_load_dwordx4 v[36:39], v1, s[6:7] nt
	s_add_u32 s6, s6, 0x400
	s_addc_u32 s7, s7, 0
	global_load_dwordx4 v[40:43], v1, s[6:7] nt
	s_add_u32 s6, s6, 0x400
	s_addc_u32 s7, s7, 0
	global_load_dwordx4 v[44:47], v1, s[6:7] nt
	s_add_u32 s6, s6, 0x400
	s_addc_u32 s7, s7, 0
	global_load_dwordx4 v[48:51], v1, s[6:7] nt
	s_add_u32 s6, s6, 0x400
	s_addc_u32 s7, s7, 0
	global_load_dwordx4 v[52:55], v1, s[6:7] nt
	s_add_u32 s6, s6, 0x400
	s_addc_u32 s7, s7, 0
	global_load_dwordx4 v[56:59], v1, s[6:7] nt
	s_add_u32 s6, s6, 0x400
	s_addc_u32 s7, s7, 0
	global_load_dwordx4 v[60:63], v1, s[6:7] nt
	s_add_u32 s6, s6, 0x400
	s_addc_u32 s7, s7, 0
	global_load_dwordx4 v[64:67], v1, s[6:7] nt
	s_add_u32 s6, s6, 0x400
	s_addc_u32 s7, s7, 0
	global_load_dwordx4 v[68:71], v1, s[6:7] nt
	s_add_u32 s6, s6, 0x400
	s_addc_u32 s7, s7, 0
	global_load_dwordx4 v[72:75], v1, s[6:7] nt
	s_add_u32 s6, s6, 0x400
	s_addc_u32 s7, s7, 0
	global_load_dwordx4 v[76:79], v1, s[6:7] nt
	s_add_u32 s6, s6, 0x400
	s_addc_u32 s7, s7, 0
	global_load_dwordx4 v[80:83], v1, s[6:7] nt
	s_add_u32 s6, s6, 0x400
	s_addc_u32 s7, s7, 0
	global_load_dwordx4 v[84:87], v1, s[6:7] nt
	s_add_u32 s6, s6, 0x400
	s_addc_u32 s7, s7, 0
	global_load_dwordx4 v[88:91], v1, s[6:7] nt
	s_add_u32 s6, s6, 0x400
	s_addc_u32 s7, s7, 0
	s_mov_b32 s26, 18
	s_add_u32 s57, s52, s51
	s_add_u32 s57, s57, 128
	s_mul_i32 s57, s57, 0x4000
	s_lshr_b32 s58, s57, 2
	s_add_u32 s6, s4, s57
	s_addc_u32 s7, s5, 0

.Lk1_contm_0:
	global_load_dwordx4 v[28:31], v1, s[6:7] nt
	s_add_u32 s6, s6, 0x400
	s_addc_u32 s7, s7, 0
	s_waitcnt vmcnt(15)
	v_or3_b32 v12, v32, v33, v34
	v_or_b32_e32 v12, v12, v35
	v_cmp_ne_u32_e32 vcc, 0, v12
	s_cbranch_vccnz .Lk1_hitm_1
.Lk1_contm_1:
	global_load_dwordx4 v[32:35], v1, s[6:7] nt
	s_add_u32 s6, s6, 0x400
	s_addc_u32 s7, s7, 0
	s_waitcnt vmcnt(15)
	v_or3_b32 v12, v36, v37, v38
	v_or_b32_e32 v12, v12, v39
	v_cmp_ne_u32_e32 vcc, 0, v12
	s_cbranch_vccnz .Lk1_hitm_2
.Lk1_contm_2:
	global_load_dwordx4 v[36:39], v1, s[6:7] nt
	s_add_u32 s6, s6, 0x400
	s_addc_u32 s7, s7, 0
	s_waitcnt vmcnt(15)
	v_or3_b32 v12, v40, v41, v42
	v_or_b32_e32 v12, v12, v43
	v_cmp_ne_u32_e32 vcc, 0, v12
	s_cbranch_vccnz .Lk1_hitm_3
.Lk1_contm_3:
	global_load_dwordx4 v[40:43], v1, s[6:7] nt
	s_add_u32 s6, s6, 0x400
	s_addc_u32 s7, s7, 0
	s_waitcnt vmcnt(15)
	v_or3_b32 v12, v44, v45, v46
	v_or_b32_e32 v12, v12, v47
	v_cmp_ne_u32_e32 vcc, 0, v12
	s_cbranch_vccnz .Lk1_hitm_4
.Lk1_contm_4:
	global_load_dwordx4 v[44:47], v1, s[6:7] nt
	s_add_u32 s6, s6, 0x400
	s_addc_u32 s7, s7, 0
	s_waitcnt vmcnt(15)
	v_or3_b32 v12, v48, v49, v50
	v_or_b32_e32 v12, v12, v51
	v_cmp_ne_u32_e32 vcc, 0, v12
	s_cbranch_vccnz .Lk1_hitm_5
.Lk1_contm_5:
	global_load_dwordx4 v[48:51], v1, s[6:7] nt
	s_add_u32 s6, s6, 0x400
	s_addc_u32 s7, s7, 0
	s_waitcnt vmcnt(15)
	v_or3_b32 v12, v52, v53, v54
	v_or_b32_e32 v12, v12, v55
	v_cmp_ne_u32_e32 vcc, 0, v12
	s_cbranch_vccnz .Lk1_hitm_6
.Lk1_contm_6:
	global_load_dwordx4 v[52:55], v1, s[6:7] nt
	s_add_u32 s6, s6, 0x400
	s_addc_u32 s7, s7, 0
	s_waitcnt vmcnt(15)
	v_or3_b32 v12, v56, v57, v58
	v_or_b32_e32 v12, v12, v59
	v_cmp_ne_u32_e32 vcc, 0, v12
	s_cbranch_vccnz .Lk1_hitm_7
.Lk1_contm_7:
	global_load_dwordx4 v[56:59], v1, s[6:7] nt
	s_add_u32 s6, s6, 0x400
	s_addc_u32 s7, s7, 0
	s_waitcnt vmcnt(15)
	v_or3_b32 v12, v60, v61, v62
	v_or_b32_e32 v12, v12, v63
	v_cmp_ne_u32_e32 vcc, 0, v12
	s_cbranch_vccnz .Lk1_hitm_8
.Lk1_contm_8:
	global_load_dwordx4 v[60:63], v1, s[6:7] nt
	s_add_u32 s6, s6, 0x400
	s_addc_u32 s7, s7, 0
	s_waitcnt vmcnt(15)
	v_or3_b32 v12, v64, v65, v66
	v_or_b32_e32 v12, v12, v67
	v_cmp_ne_u32_e32 vcc, 0, v12
	s_cbranch_vccnz .Lk1_hitm_9
.Lk1_contm_9:
	global_load_dwordx4 v[64:67], v1, s[6:7] nt
	s_add_u32 s6, s6, 0x400
	s_addc_u32 s7, s7, 0
	s_waitcnt vmcnt(15)
	v_or3_b32 v12, v68, v69, v70
	v_or_b32_e32 v12, v12, v71
	v_cmp_ne_u32_e32 vcc, 0, v12
	s_cbranch_vccnz .Lk1_hitm_10
.Lk1_contm_10:
	global_load_dwordx4 v[68:71], v1, s[6:7] nt
	s_add_u32 s6, s6, 0x400
	s_addc_u32 s7, s7, 0
	s_waitcnt vmcnt(15)
	v_or3_b32 v12, v72, v73, v74
	v_or_b32_e32 v12, v12, v75
	v_cmp_ne_u32_e32 vcc, 0, v12
	s_cbranch_vccnz .Lk1_hitm_11
.Lk1_contm_11:
	global_load_dwordx4 v[72:75], v1, s[6:7] nt
	s_add_u32 s6, s6, 0x400
	s_addc_u32 s7, s7, 0
	s_waitcnt vmcnt(15)
	v_or3_b32 v12, v76, v77, v78
	v_or_b32_e32 v12, v12, v79
	v_cmp_ne_u32_e32 vcc, 0, v12
	s_cbranch_vccnz .Lk1_hitm_12
.Lk1_contm_12:
	global_load_dwordx4 v[76:79], v1, s[6:7] nt
	s_add_u32 s6, s6, 0x400
	s_addc_u32 s7, s7, 0
	s_waitcnt vmcnt(15)
	v_or3_b32 v12, v80, v81, v82
	v_or_b32_e32 v12, v12, v83
	v_cmp_ne_u32_e32 vcc, 0, v12
	s_cbranch_vccnz .Lk1_hitm_13
.Lk1_contm_13:
	global_load_dwordx4 v[80:83], v1, s[6:7] nt
	s_add_u32 s6, s6, 0x400
	s_addc_u32 s7, s7, 0
	s_waitcnt vmcnt(15)
	v_or3_b32 v12, v84, v85, v86
	v_or_b32_e32 v12, v12, v87
	v_cmp_ne_u32_e32 vcc, 0, v12
	s_cbranch_vccnz .Lk1_hitm_14
.Lk1_contm_14:
	global_load_dwordx4 v[84:87], v1, s[6:7] nt
	s_add_u32 s6, s6, 0x400
	s_addc_u32 s7, s7, 0
	s_waitcnt vmcnt(15)
	v_or3_b32 v12, v88, v89, v90
	v_or_b32_e32 v12, v12, v91
	v_cmp_ne_u32_e32 vcc, 0, v12
	s_cbranch_vccnz .Lk1_hitm_15
.Lk1_contm_15:
	global_load_dwordx4 v[88:91], v1, s[6:7] nt
	s_add_u32 s6, s6, 0x400
	s_addc_u32 s7, s7, 0
	s_mov_b32 s18, s58
	v_readfirstlane_b32 s56, v26
	s_nop 0
	s_add_u32 s56, s56, 256
	s_cmp_lt_u32 s56, 2304
	s_cbranch_scc0 .Lk1_lastchunk
	s_add_u32 s57, s52, s56
	s_mul_i32 s57, s57, 0x4000
	s_lshr_b32 s58, s57, 2
	s_add_u32 s6, s4, s57
	s_addc_u32 s7, s5, 0
	s_mov_b64 exec, 1
	global_atomic_add v26, v27, v21, s[54:55] sc0
	s_mov_b64 exec, -1
	s_branch .Lk1_main

.Lk1_hitl_1:
	v_mov_b32_e32 v8, v32
	v_mov_b32_e32 v9, v33
	v_mov_b32_e32 v10, v34
	v_mov_b32_e32 v11, v35
	s_add_u32 s19, s18, 0x100
	s_movk_i32 s23, 17
	s_branch .Lk1_slow
.Lk1_hitl_2:
	v_mov_b32_e32 v8, v36
	v_mov_b32_e32 v9, v37
	v_mov_b32_e32 v10, v38
	v_mov_b32_e32 v11, v39
	s_add_u32 s19, s18, 0x200
	s_movk_i32 s23, 18
	s_branch .Lk1_slow
.Lk1_hitl_3:
	v_mov_b32_e32 v8, v40
	v_mov_b32_e32 v9, v41
	v_mov_b32_e32 v10, v42
	v_mov_b32_e32 v11, v43
	s_add_u32 s19, s18, 0x300
	s_movk_i32 s23, 19
	s_branch .Lk1_slow
.Lk1_hitl_4:
	v_mov_b32_e32 v8, v44
	v_mov_b32_e32 v9, v45
	v_mov_b32_e32 v10, v46
	v_mov_b32_e32 v11, v47
	s_add_u32 s19, s18, 0x400
	s_movk_i32 s23, 20
	s_branch .Lk1_slow
.Lk1_hitl_5:
	v_mov_b32_e32 v8, v48
	v_mov_b32_e32 v9, v49
	v_mov_b32_e32 v10, v50
	v_mov_b32_e32 v11, v51
	s_add_u32 s19, s18, 0x500
	s_movk_i32 s23, 21
	s_branch .Lk1_slow
.Lk1_hitl_6:
	v_mov_b32_e32 v8, v52
	v_mov_b32_e32 v9, v53
	v_mov_b32_e32 v10, v54
	v_mov_b32_e32 v11, v55
	s_add_u32 s19, s18, 0x600
	s_movk_i32 s23, 22
	s_branch .Lk1_slow
.Lk1_hitl_7:
	v_mov_b32_e32 v8, v56
	v_mov_b32_e32 v9, v57
	v_mov_b32_e32 v10, v58
	v_mov_b32_e32 v11, v59
	s_add_u32 s19, s18, 0x700
	s_movk_i32 s23, 23
	s_branch .Lk1_slow
.Lk1_hitl_8:
	v_mov_b32_e32 v8, v60
	v_mov_b32_e32 v9, v61
	v_mov_b32_e32 v10, v62
	v_mov_b32_e32 v11, v63
	s_add_u32 s19, s18, 0x800
	s_movk_i32 s23, 24
	s_branch .Lk1_slow
.Lk1_hitl_9:
	v_mov_b32_e32 v8, v64
	v_mov_b32_e32 v9, v65
	v_mov_b32_e32 v10, v66
	v_mov_b32_e32 v11, v67
	s_add_u32 s19, s18, 0x900
	s_movk_i32 s23, 25
	s_branch .Lk1_slow
.Lk1_hitl_10:
	v_mov_b32_e32 v8, v68
	v_mov_b32_e32 v9, v69
	v_mov_b32_e32 v10, v70
	v_mov_b32_e32 v11, v71
	s_add_u32 s19, s18, 0xa00
	s_movk_i32 s23, 26
	s_branch .Lk1_slow
.Lk1_hitl_11:
	v_mov_b32_e32 v8, v72
	v_mov_b32_e32 v9, v73
	v_mov_b32_e32 v10, v74
	v_mov_b32_e32 v11, v75
	s_add_u32 s19, s18, 0xb00
	s_movk_i32 s23, 27
	s_branch .Lk1_slow
.Lk1_hitl_12:
	v_mov_b32_e32 v8, v76
	v_mov_b32_e32 v9, v77
	v_mov_b32_e32 v10, v78
	v_mov_b32_e32 v11, v79
	s_add_u32 s19, s18, 0xc00
	s_movk_i32 s23, 28
	s_branch .Lk1_slow
.Lk1_hitl_13:
	v_mov_b32_e32 v8, v80
	v_mov_b32_e32 v9, v81
	v_mov_b32_e32 v10, v82
	v_mov_b32_e32 v11, v83
	s_add_u32 s19, s18, 0xd00
	s_movk_i32 s23, 29
	s_branch .Lk1_slow
.Lk1_hitl_14:
	v_mov_b32_e32 v8, v84
	v_mov_b32_e32 v9, v85
	v_mov_b32_e32 v10, v86
	v_mov_b32_e32 v11, v87
	s_add_u32 s19, s18, 0xe00
	s_movk_i32 s23, 30
	s_branch .Lk1_slow
.Lk1_hitl_15:
	v_mov_b32_e32 v8, v88
	v_mov_b32_e32 v9, v89
	v_mov_b32_e32 v10, v90
	v_mov_b32_e32 v11, v91
	s_add_u32 s19, s18, 0xf00
	s_movk_i32 s23, 31
	s_branch .Lk1_slow

_Z10agg_kernelILi128ELb1EEvPKiPKfP15HIP_vector_typeIiLj2EES6_PKDF16_S3_PDF16_Pf:
	s_cmp_lg_u32 s2, 0
	s_cbranch_scc1 .Lagg_zc_skip
	s_load_dwordx2 s[6:7], s[0:1], 0x38
	v_lshlrev_b32_e32 v2, 4, v0
	v_mov_b32_e32 v4, 0
	v_mov_b32_e32 v5, 0
	v_mov_b32_e32 v6, 0
	v_mov_b32_e32 v7, 0
	v_cmp_gt_u32_e32 vcc, 64, v0
	s_waitcnt lgkmcnt(0)
	s_add_u32 s6, s6, 0x2000
	s_addc_u32 s7, s7, 0
	s_and_saveexec_b64 s[4:5], vcc
	global_store_dwordx4 v2, v[4:7], s[6:7]
	s_mov_b64 exec, s[4:5]
.Lagg_zc_skip:
	s_load_dwordx4 s[12:15], s[0:1], 0x0
	s_load_dwordx2 s[24:25], s[0:1], 0x10
	s_load_dwordx4 s[20:23], s[0:1], 0x20
	s_mov_b32 s10, s2
	v_lshrrev_b32_e32 v1, 6, v0
	s_lshl_b32 s2, s2, 4
	v_lshl_or_b32 v30, v1, 1, s2
	v_and_b32_e32 v54, 15, v0
	v_lshlrev_b32_e32 v76, 3, v54
	v_ashrrev_i32_e32 v31, 31, v30
	v_bfe_u32 v75, v0, 4, 2
	v_lshlrev_b64 v[10:11], 2, v[30:31]
	v_lshl_or_b32 v42, v30, 7, v76
	v_mov_b32_e32 v43, 0
	v_lshlrev_b32_e32 v1, 6, v30
	v_lshlrev_b32_e32 v74, 5, v54
	s_waitcnt lgkmcnt(0)
	v_lshl_add_u64 v[34:35], s[12:13], 0, v[10:11]
	v_lshl_add_u64 v[36:37], s[14:15], 0, v[10:11]
	v_lshl_add_u64 v[10:11], v[42:43], 1, s[20:21]
	v_or_b32_e32 v14, v75, v1
	v_mov_b32_e32 v15, v43
	global_load_dwordx4 v[2:5], v74, s[22:23] offset:16
	global_load_dwordx4 v[6:9], v74, s[22:23]
	v_lshl_add_u64 v[46:47], v[14:15], 3, s[24:25]
	global_load_dwordx4 v[10:13], v[10:11], off
	v_mov_b32_e32 v49, v43
	global_load_dword v79, v[34:35], off
	global_load_dword v78, v[36:37], off
	global_load_dwordx2 v[40:41], v[46:47], off offset:32
	global_load_dwordx2 v[38:39], v[46:47], off offset:64
	global_load_dwordx2 v[32:33], v[46:47], off offset:96
	v_mov_b32_e32 v48, v30
	s_waitcnt vmcnt(5)
	v_mov_b64_e32 v[24:25], v[12:13]
	v_mov_b64_e32 v[22:23], v[10:11]
	s_waitcnt vmcnt(4)
	v_cmp_lt_i32_e64 s[4:5], v75, v79
	s_waitcnt vmcnt(3)
	v_mov_b32_e32 v55, v78
	s_and_saveexec_b64 s[2:3], s[4:5]
	s_cbranch_execz .LBB3_2
	global_load_dwordx2 v[48:49], v[46:47], off
	v_mov_b32_e32 v15, 0
	s_waitcnt vmcnt(0)
	v_ashrrev_i32_e32 v17, 31, v48
	v_mov_b32_e32 v16, v48
	v_lshl_or_b32 v14, v48, 7, v76
	v_lshl_add_u64 v[16:17], v[16:17], 2, s[14:15]
	v_lshl_add_u64 v[14:15], v[14:15], 1, s[20:21]
	global_load_dword v55, v[16:17], off
	global_load_dwordx4 v[22:25], v[14:15], off
